# P0 expert loop: each item's 4 fp8 stores deferred (copied to spare VGPRs) and issued right after the next half's load burst so in-order vmcnt waits never sit on fresh store acks; both waits vmcnt(63)
# baseline (speedup 1.0000x reference)
; #define LAS __attribute__((address_space(3)))
; __global__ void __launch_bounds__(512, 2) fwd(Args args) {
;     extern __shared__ __attribute__((aligned(16))) unsigned char lds_raw[];
;     Frame F;
;     F.lds = (LAS unsigned char*)lds_raw;
;     F.MISC = (volatile LAS unsigned*)(F.lds + MISC_OFF);
;     F.tid = threadIdx.x; F.lane = F.tid & 63; F.wave = __builtin_amdgcn_readfirstlane(F.tid >> 6);
;     F.G = gridDim.x; { const int bx = blockIdx.x; F.vcu = (F.G % 8 == 0) ? (bx % 8) * (F.G / 8) + bx / 8 : bx; }
;     F.ws = args.ws; F.ctl = (gu32*)(args.ws + WS_CTL); F.out = args.out;
_Z3fwd4Args:
	s_mov_b64 s[100:101], 0
	s_load_dword s33, s[0:1], 0xf8
	s_add_u32 s4, s0, 0xf8
	s_addc_u32 s5, s1, 0
	v_readfirstlane_b32 s3, v0
	v_writelane_b32 v255, s4, 0
	s_nop 1
	v_writelane_b32 v255, s5, 1
	s_waitcnt lgkmcnt(0)
	s_and_b32 s4, s33, 7
	s_cmp_lg_u32 s4, 0
	v_writelane_b32 v255, s2, 2
	s_cbranch_scc1 .LBB0_2
	s_ashr_i32 s5, s2, 31
	s_lshr_b32 s5, s5, 29
	s_add_i32 s5, s2, s5
	s_and_b32 s6, s5, -8
	s_ashr_i32 s4, s33, 3
	s_sub_i32 s6, s2, s6
	s_mul_i32 s4, s4, s6
	s_ashr_i32 s5, s5, 3
	s_add_i32 s4, s4, s5
	v_writelane_b32 v255, s4, 2

; #define MOE_LOAD(v, it) do { _Pragma("unroll") for (int i_ = 0; i_ < 64; ++i_) v[i_] = __builtin_nontemporal_load((it).src + (size_t)(2 * i_) * (it).stride); } while (0)
;     ...
;             ia = moe_item(wg, wu, wd, win, wout, wpn, wpd, F.ws, it2 <= last ? it2 : last, F.lane); MOE_LOAD(va, ia);
;             MOE_PROC(vb, ib);
.LBB0_80:
	s_lshl_b64 s[68:69], s[68:69], 3
	v_lshl_add_u64 v[14:15], v[16:17], 0, s[68:69]
	global_load_dword v87, v[16:17], off nt
	v_lshl_add_u64 v[16:17], v[14:15], 0, s[68:69]
	v_lshl_add_u64 v[30:31], v[16:17], 0, s[68:69]
	v_lshl_add_u64 v[32:33], v[30:31], 0, s[68:69]
	v_lshl_add_u64 v[34:35], v[32:33], 0, s[68:69]
	v_lshl_add_u64 v[36:37], v[34:35], 0, s[68:69]
	v_lshl_add_u64 v[38:39], v[36:37], 0, s[68:69]
	v_lshl_add_u64 v[40:41], v[38:39], 0, s[68:69]
	global_load_dword v92, v[14:15], off nt
	global_load_dword v91, v[16:17], off nt
	global_load_dword v90, v[30:31], off nt
	global_load_dword v89, v[32:33], off nt
	global_load_dword v88, v[34:35], off nt
	global_load_dword v86, v[36:37], off nt
	global_load_dword v85, v[38:39], off nt
	global_load_dword v83, v[40:41], off nt
	v_lshl_add_u64 v[14:15], v[40:41], 0, s[68:69]
	v_lshl_add_u64 v[16:17], v[14:15], 0, s[68:69]
	global_load_dword v84, v[14:15], off nt
	global_load_dword v79, v[16:17], off nt
	v_lshl_add_u64 v[14:15], v[16:17], 0, s[68:69]
	global_load_dword v80, v[14:15], off nt
	v_lshl_add_u64 v[14:15], v[14:15], 0, s[68:69]
	global_load_dword v75, v[14:15], off nt
	v_lshl_add_u64 v[14:15], v[14:15], 0, s[68:69]
	global_load_dword v76, v[14:15], off nt
	v_lshl_add_u64 v[14:15], v[14:15], 0, s[68:69]
	global_load_dword v71, v[14:15], off nt
	v_lshl_add_u64 v[14:15], v[14:15], 0, s[68:69]
	global_load_dword v72, v[14:15], off nt
	v_lshl_add_u64 v[14:15], v[14:15], 0, s[68:69]
	global_load_dword v65, v[14:15], off nt
	v_lshl_add_u64 v[14:15], v[14:15], 0, s[68:69]
	global_load_dword v66, v[14:15], off nt
	v_lshl_add_u64 v[14:15], v[14:15], 0, s[68:69]
	global_load_dword v61, v[14:15], off nt
	v_lshl_add_u64 v[14:15], v[14:15], 0, s[68:69]
	global_load_dword v62, v[14:15], off nt
	v_lshl_add_u64 v[14:15], v[14:15], 0, s[68:69]
	global_load_dword v57, v[14:15], off nt
	v_lshl_add_u64 v[14:15], v[14:15], 0, s[68:69]
	global_load_dword v58, v[14:15], off nt
	v_lshl_add_u64 v[14:15], v[14:15], 0, s[68:69]
	global_load_dword v53, v[14:15], off nt
	v_lshl_add_u64 v[14:15], v[14:15], 0, s[68:69]
	global_load_dword v54, v[14:15], off nt
	v_lshl_add_u64 v[14:15], v[14:15], 0, s[68:69]
	global_load_dword v45, v[14:15], off nt
	v_lshl_add_u64 v[14:15], v[14:15], 0, s[68:69]
	global_load_dword v46, v[14:15], off nt
	v_lshl_add_u64 v[14:15], v[14:15], 0, s[68:69]
	global_load_dword v35, v[14:15], off nt
	v_lshl_add_u64 v[14:15], v[14:15], 0, s[68:69]
	global_load_dword v36, v[14:15], off nt
	v_lshl_add_u64 v[14:15], v[14:15], 0, s[68:69]
	global_load_dword v33, v[14:15], off nt
	v_lshl_add_u64 v[14:15], v[14:15], 0, s[68:69]
	global_load_dword v34, v[14:15], off nt
	v_lshl_add_u64 v[14:15], v[14:15], 0, s[68:69]
	global_load_dword v31, v[14:15], off nt
	v_lshl_add_u64 v[14:15], v[14:15], 0, s[68:69]
	global_load_dword v32, v[14:15], off nt
	v_lshl_add_u64 v[14:15], v[14:15], 0, s[68:69]
	global_load_dword v29, v[14:15], off nt
	v_lshl_add_u64 v[14:15], v[14:15], 0, s[68:69]
	global_load_dword v30, v[14:15], off nt
	v_lshl_add_u64 v[14:15], v[14:15], 0, s[68:69]
	global_load_dword v81, v[14:15], off nt
	v_lshl_add_u64 v[14:15], v[14:15], 0, s[68:69]
	global_load_dword v82, v[14:15], off nt
	v_lshl_add_u64 v[14:15], v[14:15], 0, s[68:69]
	global_load_dword v77, v[14:15], off nt
	v_lshl_add_u64 v[14:15], v[14:15], 0, s[68:69]
	global_load_dword v78, v[14:15], off nt
	v_lshl_add_u64 v[14:15], v[14:15], 0, s[68:69]
	global_load_dword v73, v[14:15], off nt
	v_lshl_add_u64 v[14:15], v[14:15], 0, s[68:69]
	global_load_dword v74, v[14:15], off nt
	v_lshl_add_u64 v[14:15], v[14:15], 0, s[68:69]
	global_load_dword v69, v[14:15], off nt
	v_lshl_add_u64 v[14:15], v[14:15], 0, s[68:69]
	global_load_dword v70, v[14:15], off nt
	v_lshl_add_u64 v[14:15], v[14:15], 0, s[68:69]
	global_load_dword v67, v[14:15], off nt
	v_lshl_add_u64 v[14:15], v[14:15], 0, s[68:69]
	global_load_dword v68, v[14:15], off nt
	v_lshl_add_u64 v[14:15], v[14:15], 0, s[68:69]
	global_load_dword v63, v[14:15], off nt
	v_lshl_add_u64 v[14:15], v[14:15], 0, s[68:69]
	global_load_dword v64, v[14:15], off nt
	v_lshl_add_u64 v[14:15], v[14:15], 0, s[68:69]
	global_load_dword v59, v[14:15], off nt
	v_lshl_add_u64 v[14:15], v[14:15], 0, s[68:69]
	global_load_dword v60, v[14:15], off nt
	v_lshl_add_u64 v[14:15], v[14:15], 0, s[68:69]
	global_load_dword v55, v[14:15], off nt
	v_lshl_add_u64 v[14:15], v[14:15], 0, s[68:69]
	global_load_dword v56, v[14:15], off nt
	v_lshl_add_u64 v[14:15], v[14:15], 0, s[68:69]
	global_load_dword v51, v[14:15], off nt
	v_lshl_add_u64 v[14:15], v[14:15], 0, s[68:69]
	global_load_dword v52, v[14:15], off nt
	v_lshl_add_u64 v[14:15], v[14:15], 0, s[68:69]
	global_load_dword v38, v[14:15], off nt
	v_lshl_add_u64 v[14:15], v[14:15], 0, s[68:69]
	global_load_dword v39, v[14:15], off nt
	v_lshl_add_u64 v[14:15], v[14:15], 0, s[68:69]
	global_load_dword v40, v[14:15], off nt
	v_lshl_add_u64 v[14:15], v[14:15], 0, s[68:69]
	global_load_dword v42, v[14:15], off nt
	v_lshl_add_u64 v[14:15], v[14:15], 0, s[68:69]
	global_load_dword v37, v[14:15], off nt
	v_lshl_add_u64 v[14:15], v[14:15], 0, s[68:69]
	global_load_dword v41, v[14:15], off nt
	v_lshl_add_u64 v[14:15], v[14:15], 0, s[68:69]
	global_load_dword v43, v[14:15], off nt
	v_lshl_add_u64 v[14:15], v[14:15], 0, s[68:69]
	global_load_dword v44, v[14:15], off nt
	v_lshl_add_u64 v[14:15], v[14:15], 0, s[68:69]
	global_load_dword v47, v[14:15], off nt
	v_lshl_add_u64 v[14:15], v[14:15], 0, s[68:69]
	global_load_dword v48, v[14:15], off nt
	v_lshl_add_u64 v[14:15], v[14:15], 0, s[68:69]
	global_load_dword v49, v[14:15], off nt
	v_lshl_add_u64 v[14:15], v[14:15], 0, s[68:69]
	global_store_dwordx4 v[196:197], v[204:207], off
	global_store_dwordx4 v[198:199], v[208:211], off
	global_store_dwordx4 v[200:201], v[212:215], off
	global_store_dwordx4 v[202:203], v[216:219], off
	s_waitcnt vmcnt(63)
	ds_write2st64_b32 v28, v93, v101 offset1:1
	ds_write2st64_b32 v28, v99, v100 offset0:2 offset1:3
	ds_write2st64_b32 v28, v97, v98 offset0:4 offset1:5
	ds_write2st64_b32 v28, v95, v96 offset0:6 offset1:7
	ds_write2st64_b32 v21, v94, v124 offset0:8 offset1:9
	ds_write2st64_b32 v21, v104, v114 offset0:10 offset1:11
	ds_write2st64_b32 v21, v105, v115 offset0:12 offset1:13
	ds_write2st64_b32 v21, v106, v116 offset0:14 offset1:15
	ds_write2st64_b32 v22, v107, v117 offset0:16 offset1:17
	ds_write2st64_b32 v22, v108, v118 offset0:18 offset1:19
	ds_write2st64_b32 v22, v109, v119 offset0:20 offset1:21
	ds_write2st64_b32 v22, v110, v120 offset0:22 offset1:23
	ds_write2st64_b32 v23, v111, v121 offset0:24 offset1:25
	ds_write2st64_b32 v23, v112, v122 offset0:26 offset1:27
	global_load_dword v50, v[14:15], off nt
	ds_write2st64_b32 v23, v102, v103 offset0:28 offset1:29
	ds_write2st64_b32 v23, v113, v123 offset0:30 offset1:31
	ds_write2st64_b32 v24, v125, v126 offset0:32 offset1:33
	ds_write2st64_b32 v24, v127, v128 offset0:34 offset1:35
	ds_write2st64_b32 v24, v129, v130 offset0:36 offset1:37
	ds_write2st64_b32 v24, v131, v132 offset0:38 offset1:39
	ds_write2st64_b32 v25, v133, v134 offset0:40 offset1:41
	ds_write2st64_b32 v25, v135, v136 offset0:42 offset1:43
	ds_write2st64_b32 v25, v137, v138 offset0:44 offset1:45
	ds_write2st64_b32 v25, v139, v140 offset0:46 offset1:47
	ds_write2st64_b32 v26, v141, v142 offset0:48 offset1:49
	ds_write2st64_b32 v26, v143, v144 offset0:50 offset1:51
	ds_write2st64_b32 v26, v146, v147 offset0:52 offset1:53
	ds_write2st64_b32 v26, v148, v149 offset0:54 offset1:55
	ds_write2st64_b32 v27, v151, v152 offset0:56 offset1:57
	ds_write2st64_b32 v27, v153, v154 offset0:58 offset1:59
	ds_write2st64_b32 v27, v155, v157 offset0:60 offset1:61
	ds_write2st64_b32 v27, v158, v159 offset0:62 offset1:63
	s_waitcnt lgkmcnt(0)
	ds_read2_b32 v[16:17], v1 offset1:32
	v_lshlrev_b64 v[14:15], s44, v[2:3]
	v_lshl_add_u64 v[12:13], v[12:13], 0, v[14:15]
	v_lshl_add_u64 v[98:99], v[12:13], 0, v[6:7]
	v_mov_b32_e32 v12, 0
	s_waitcnt lgkmcnt(0)
	v_mul_f32_e32 v4, 0x42800000, v16
	v_mul_f32_e32 v13, 0x42800000, v17
	ds_read2_b32 v[16:17], v1 offset0:64 offset1:96
	ds_read2_b32 v[94:95], v1 offset0:128 offset1:160
	v_cvt_pk_fp8_f32 v12, v4, v13
	v_lshlrev_b64 v[14:15], s46, v[2:3]
	v_lshl_add_u64 v[10:11], v[10:11], 0, v[14:15]
	s_waitcnt lgkmcnt(1)
	v_mul_f32_e32 v4, 0x42800000, v16
	v_mul_f32_e32 v13, 0x42800000, v17
	v_cvt_pk_fp8_f32 v12, v4, v13 op_sel:[0,0,1]
	s_waitcnt lgkmcnt(0)
	v_mul_f32_e32 v4, 0x42800000, v94
	ds_read2_b32 v[14:15], v1 offset0:192 offset1:224
	v_mul_f32_e32 v16, 0x42800000, v95
	v_mov_b32_e32 v13, 0
	v_cvt_pk_fp8_f32 v13, v4, v16
	ds_read2_b32 v[16:17], v145 offset1:32
	s_waitcnt lgkmcnt(1)
	v_mul_f32_e32 v4, 0x42800000, v14
	v_mul_f32_e32 v93, 0x42800000, v15
	ds_read2_b32 v[14:15], v145 offset0:64 offset1:96
	v_cvt_pk_fp8_f32 v13, v4, v93 op_sel:[0,0,1]
	s_waitcnt lgkmcnt(1)
	v_mul_f32_e32 v4, 0x42800000, v16
	v_mul_f32_e32 v93, 0x42800000, v17
	ds_read2_b32 v[16:17], v145 offset0:128 offset1:160
	s_waitcnt lgkmcnt(1)
	v_mul_f32_e32 v96, 0x42800000, v14
	v_mov_b32_e32 v14, 0
	v_cvt_pk_fp8_f32 v14, v4, v93
	v_mul_f32_e32 v97, 0x42800000, v15
	s_waitcnt lgkmcnt(0)
	v_mul_f32_e32 v4, 0x42800000, v16
	v_mul_f32_e32 v93, 0x42800000, v17
	ds_read2_b32 v[16:17], v145 offset0:192 offset1:224
	v_mov_b32_e32 v15, 0
	v_cvt_pk_fp8_f32 v15, v4, v93
	ds_read2_b32 v[94:95], v9 offset1:32
	v_cvt_pk_fp8_f32 v14, v96, v97 op_sel:[0,0,1]
	s_waitcnt lgkmcnt(1)
	v_mul_f32_e32 v4, 0x42800000, v16
	v_mul_f32_e32 v16, 0x42800000, v17
	v_cvt_pk_fp8_f32 v15, v4, v16 op_sel:[0,0,1]
	ds_read2_b32 v[16:17], v9 offset0:64 offset1:96
	s_waitcnt lgkmcnt(1)
	v_mul_f32_e32 v4, 0x42800000, v94
	v_mul_f32_e32 v93, 0x42800000, v95
	v_mov_b32_e32 v94, 0
	ds_read2_b32 v[96:97], v9 offset0:128 offset1:160
	v_cvt_pk_fp8_f32 v94, v4, v93
	s_nop 0
	v_mov_b64_e32 v[172:173], v[98:99]
	v_mov_b64_e32 v[180:181], v[12:13]
	v_mov_b64_e32 v[182:183], v[14:15]
	s_waitcnt lgkmcnt(1)
	v_mul_f32_e32 v4, 0x42800000, v16
	v_mov_b32_e32 v95, 0
	v_mul_f32_e32 v12, 0x42800000, v17
	v_cvt_pk_fp8_f32 v94, v4, v12 op_sel:[0,0,1]
	s_waitcnt lgkmcnt(0)
	v_mul_f32_e32 v4, 0x42800000, v96
	ds_read2_b32 v[12:13], v9 offset0:192 offset1:224
	v_mul_f32_e32 v14, 0x42800000, v97
	v_cvt_pk_fp8_f32 v95, v4, v14
	ds_read2_b32 v[14:15], v150 offset1:32
	v_mov_b32_e32 v96, 0
	s_waitcnt lgkmcnt(1)
;     ...
;         for (int j = 0; j < nmine; j += 2) {
	v_mul_f32_e32 v4, 0x42800000, v12
	v_mul_f32_e32 v16, 0x42800000, v13
	ds_read2_b32 v[12:13], v150 offset0:64 offset1:96
	v_cvt_pk_fp8_f32 v95, v4, v16 op_sel:[0,0,1]
	s_waitcnt lgkmcnt(1)
	v_mul_f32_e32 v4, 0x42800000, v14
	v_mul_f32_e32 v16, 0x42800000, v15
	ds_read2_b32 v[14:15], v150 offset0:128 offset1:160
	s_waitcnt lgkmcnt(1)
	v_mul_f32_e32 v17, 0x42800000, v12
	v_mul_f32_e32 v93, 0x42800000, v13
	ds_read2_b32 v[12:13], v150 offset0:192 offset1:224
	v_cvt_pk_fp8_f32 v96, v4, v16
	s_waitcnt lgkmcnt(1)
	v_mul_f32_e32 v4, 0x42800000, v14
	v_mul_f32_e32 v14, 0x42800000, v15
	v_mov_b32_e32 v97, 0
	v_cvt_pk_fp8_f32 v97, v4, v14
	s_waitcnt lgkmcnt(0)
	v_mul_f32_e32 v4, 0x42800000, v12
	v_mul_f32_e32 v12, 0x42800000, v13
	v_cvt_pk_fp8_f32 v96, v17, v93 op_sel:[0,0,1]
	v_cvt_pk_fp8_f32 v97, v4, v12 op_sel:[0,0,1]
	s_lshl_b32 s4, s42, 3
	ds_read2_b32 v[12:13], v18 offset1:32
	v_lshl_add_u64 v[16:17], v[98:99], 0, s[4:5]
	ds_read2_b32 v[14:15], v18 offset0:64 offset1:96
	s_nop 0
	v_mov_b64_e32 v[174:175], v[16:17]
	v_mov_b64_e32 v[184:185], v[94:95]
	v_mov_b64_e32 v[186:187], v[96:97]
	ds_read2_b32 v[94:95], v18 offset0:128 offset1:160
	s_waitcnt lgkmcnt(2)
	v_mul_f32_e32 v4, 0x42800000, v12
	v_mul_f32_e32 v13, 0x42800000, v13
	v_mov_b32_e32 v12, 0
	s_waitcnt lgkmcnt(1)
	v_mul_f32_e32 v93, 0x42800000, v14
	v_mul_f32_e32 v96, 0x42800000, v15
	v_cvt_pk_fp8_f32 v12, v4, v13
	s_waitcnt lgkmcnt(0)
	v_mul_f32_e32 v4, 0x42800000, v94
	v_mul_f32_e32 v94, 0x42800000, v95
	ds_read2_b32 v[14:15], v18 offset0:192 offset1:224
	v_mov_b32_e32 v13, 0
	v_cvt_pk_fp8_f32 v13, v4, v94
	ds_read2_b32 v[94:95], v156 offset1:32
	v_cvt_pk_fp8_f32 v12, v93, v96 op_sel:[0,0,1]
	s_waitcnt lgkmcnt(1)
	v_mul_f32_e32 v4, 0x42800000, v14
	v_mul_f32_e32 v14, 0x42800000, v15
	ds_read2_b32 v[96:97], v156 offset0:64 offset1:96
	v_cvt_pk_fp8_f32 v13, v4, v14 op_sel:[0,0,1]
	s_waitcnt lgkmcnt(1)
	v_mul_f32_e32 v4, 0x42800000, v94
	v_mul_f32_e32 v15, 0x42800000, v95
	v_mov_b32_e32 v14, 0
	ds_read2_b32 v[94:95], v156 offset0:128 offset1:160
	v_cvt_pk_fp8_f32 v14, v4, v15
	s_waitcnt lgkmcnt(1)
	v_mul_f32_e32 v4, 0x42800000, v96
	v_mul_f32_e32 v15, 0x42800000, v97
	ds_read2_b32 v[96:97], v156 offset0:192 offset1:224
	v_cvt_pk_fp8_f32 v14, v4, v15 op_sel:[0,0,1]
	s_waitcnt lgkmcnt(1)
	v_mul_f32_e32 v4, 0x42800000, v94
	v_mul_f32_e32 v93, 0x42800000, v95
	ds_read2_b32 v[94:95], v19 offset1:32
	s_waitcnt lgkmcnt(1)
	v_mul_f32_e32 v100, 0x42800000, v96
	v_mul_f32_e32 v101, 0x42800000, v97
	v_mov_b32_e32 v15, 0
	ds_read2_b32 v[96:97], v19 offset0:64 offset1:96
	v_cvt_pk_fp8_f32 v15, v4, v93
	s_waitcnt lgkmcnt(1)
	v_mul_f32_e32 v4, 0x42800000, v94
	v_mul_f32_e32 v93, 0x42800000, v95
	v_mov_b32_e32 v94, 0
	ds_read2_b32 v[98:99], v19 offset0:128 offset1:160
	v_cvt_pk_fp8_f32 v94, v4, v93
	s_waitcnt lgkmcnt(1)
	v_mul_f32_e32 v4, 0x42800000, v96
	v_mul_f32_e32 v93, 0x42800000, v97
	ds_read2_b32 v[96:97], v19 offset0:192 offset1:224
	v_cvt_pk_fp8_f32 v94, v4, v93 op_sel:[0,0,1]
	s_waitcnt lgkmcnt(1)
	v_mul_f32_e32 v4, 0x42800000, v98
	v_mul_f32_e32 v93, 0x42800000, v99
	v_mov_b32_e32 v95, 0
	ds_read2_b32 v[98:99], v160 offset1:32
	v_cvt_pk_fp8_f32 v95, v4, v93
	s_waitcnt lgkmcnt(1)
	v_mul_f32_e32 v4, 0x42800000, v96
	v_mul_f32_e32 v93, 0x42800000, v97
	ds_read2_b32 v[96:97], v160 offset0:64 offset1:96
	v_cvt_pk_fp8_f32 v95, v4, v93 op_sel:[0,0,1]
	s_waitcnt lgkmcnt(1)
	v_mul_f32_e32 v4, 0x42800000, v98
	v_mul_f32_e32 v93, 0x42800000, v99
	ds_read2_b32 v[98:99], v160 offset0:128 offset1:160
	v_cvt_pk_fp8_f32 v15, v100, v101 op_sel:[0,0,1]
	s_waitcnt lgkmcnt(1)
	v_mul_f32_e32 v102, 0x42800000, v96
	v_mov_b32_e32 v96, 0
	ds_read2_b32 v[100:101], v160 offset0:192 offset1:224
	v_mul_f32_e32 v103, 0x42800000, v97
	v_cvt_pk_fp8_f32 v96, v4, v93
	s_waitcnt lgkmcnt(1)
	v_mul_f32_e32 v4, 0x42800000, v98
	v_mul_f32_e32 v93, 0x42800000, v99
	v_mov_b32_e32 v97, 0
	v_cvt_pk_fp8_f32 v97, v4, v93
	s_waitcnt lgkmcnt(0)
	v_mul_f32_e32 v4, 0x42800000, v100
	v_mul_f32_e32 v93, 0x42800000, v101
	v_cvt_pk_fp8_f32 v96, v102, v103 op_sel:[0,0,1]
	v_cvt_pk_fp8_f32 v97, v4, v93 op_sel:[0,0,1]
	v_lshl_add_u64 v[16:17], v[16:17], 0, s[4:5]
	s_nop 0
	v_mov_b64_e32 v[176:177], v[16:17]
	v_mov_b64_e32 v[188:189], v[12:13]
	v_mov_b64_e32 v[190:191], v[14:15]
	s_add_i32 s91, s91, 2
	s_cmp_ge_i32 s91, s6
	v_lshl_add_u64 v[12:13], v[16:17], 0, s[4:5]
	s_nop 0
	v_mov_b64_e32 v[178:179], v[12:13]
	v_mov_b64_e32 v[192:193], v[94:95]
	v_mov_b64_e32 v[194:195], v[96:97]
	s_waitcnt lgkmcnt(0)
	s_mov_b64 s[100:101], -1
	s_cbranch_scc1 .LBB0_130

; #define MOE_LOAD(v, it) do { _Pragma("unroll") for (int i_ = 0; i_ < 64; ++i_) v[i_] = __builtin_nontemporal_load((it).src + (size_t)(2 * i_) * (it).stride); } while (0)
;     ...
;             ib = moe_item(wg, wu, wd, win, wout, wpn, wpd, F.ws, it1 <= last ? it1 : last, F.lane); MOE_LOAD(vb, ib);
;             MOE_PROC(va, ia);
.LBB0_105:
	s_lshl_b64 s[46:47], s[46:47], 3
	global_load_dword v93, v[16:17], off nt
	v_lshl_add_u64 v[16:17], v[16:17], 0, s[46:47]
	v_lshl_add_u64 v[94:95], v[16:17], 0, s[46:47]
	v_lshl_add_u64 v[96:97], v[94:95], 0, s[46:47]
	v_lshl_add_u64 v[102:103], v[96:97], 0, s[46:47]
	v_lshl_add_u64 v[104:105], v[102:103], 0, s[46:47]
	v_lshl_add_u64 v[106:107], v[104:105], 0, s[46:47]
	v_lshl_add_u64 v[108:109], v[106:107], 0, s[46:47]
	v_lshl_add_u64 v[110:111], v[108:109], 0, s[46:47]
	global_load_dword v101, v[16:17], off nt
	global_load_dword v99, v[94:95], off nt
	global_load_dword v100, v[96:97], off nt
	s_nop 0
	global_load_dword v97, v[102:103], off nt
	global_load_dword v98, v[104:105], off nt
	global_load_dword v95, v[106:107], off nt
	global_load_dword v96, v[108:109], off nt
	global_load_dword v94, v[110:111], off nt
	v_lshl_add_u64 v[16:17], v[110:111], 0, s[46:47]
	v_lshl_add_u64 v[102:103], v[16:17], 0, s[46:47]
	global_load_dword v124, v[16:17], off nt
	global_load_dword v104, v[102:103], off nt
	v_lshl_add_u64 v[16:17], v[102:103], 0, s[46:47]
	global_load_dword v114, v[16:17], off nt
	v_lshl_add_u64 v[16:17], v[16:17], 0, s[46:47]
	global_load_dword v105, v[16:17], off nt
	v_lshl_add_u64 v[16:17], v[16:17], 0, s[46:47]
	global_load_dword v115, v[16:17], off nt
	v_lshl_add_u64 v[16:17], v[16:17], 0, s[46:47]
	global_load_dword v106, v[16:17], off nt
	v_lshl_add_u64 v[16:17], v[16:17], 0, s[46:47]
	global_load_dword v116, v[16:17], off nt
	v_lshl_add_u64 v[16:17], v[16:17], 0, s[46:47]
	global_load_dword v107, v[16:17], off nt
	v_lshl_add_u64 v[16:17], v[16:17], 0, s[46:47]
	global_load_dword v117, v[16:17], off nt
	v_lshl_add_u64 v[16:17], v[16:17], 0, s[46:47]
	global_load_dword v108, v[16:17], off nt
	v_lshl_add_u64 v[16:17], v[16:17], 0, s[46:47]
	global_load_dword v118, v[16:17], off nt
	v_lshl_add_u64 v[16:17], v[16:17], 0, s[46:47]
	global_load_dword v109, v[16:17], off nt
	v_lshl_add_u64 v[16:17], v[16:17], 0, s[46:47]
	global_load_dword v119, v[16:17], off nt
	v_lshl_add_u64 v[16:17], v[16:17], 0, s[46:47]
	global_load_dword v110, v[16:17], off nt
	v_lshl_add_u64 v[16:17], v[16:17], 0, s[46:47]
	global_load_dword v120, v[16:17], off nt
	v_lshl_add_u64 v[16:17], v[16:17], 0, s[46:47]
	global_load_dword v111, v[16:17], off nt
	v_lshl_add_u64 v[16:17], v[16:17], 0, s[46:47]
	global_load_dword v121, v[16:17], off nt
	v_lshl_add_u64 v[16:17], v[16:17], 0, s[46:47]
	global_load_dword v112, v[16:17], off nt
	v_lshl_add_u64 v[16:17], v[16:17], 0, s[46:47]
	global_load_dword v122, v[16:17], off nt
	v_lshl_add_u64 v[16:17], v[16:17], 0, s[46:47]
	global_load_dword v102, v[16:17], off nt
	v_lshl_add_u64 v[16:17], v[16:17], 0, s[46:47]
	global_load_dword v103, v[16:17], off nt
	v_lshl_add_u64 v[16:17], v[16:17], 0, s[46:47]
	global_load_dword v113, v[16:17], off nt
	v_lshl_add_u64 v[16:17], v[16:17], 0, s[46:47]
	global_load_dword v123, v[16:17], off nt
	v_lshl_add_u64 v[16:17], v[16:17], 0, s[46:47]
	global_load_dword v125, v[16:17], off nt
	v_lshl_add_u64 v[16:17], v[16:17], 0, s[46:47]
	global_load_dword v126, v[16:17], off nt
	v_lshl_add_u64 v[16:17], v[16:17], 0, s[46:47]
	global_load_dword v127, v[16:17], off nt
	v_lshl_add_u64 v[16:17], v[16:17], 0, s[46:47]
	global_load_dword v128, v[16:17], off nt
	v_lshl_add_u64 v[16:17], v[16:17], 0, s[46:47]
	global_load_dword v129, v[16:17], off nt
	v_lshl_add_u64 v[16:17], v[16:17], 0, s[46:47]
	global_load_dword v130, v[16:17], off nt
	v_lshl_add_u64 v[16:17], v[16:17], 0, s[46:47]
	global_load_dword v131, v[16:17], off nt
	v_lshl_add_u64 v[16:17], v[16:17], 0, s[46:47]
	global_load_dword v132, v[16:17], off nt
	v_lshl_add_u64 v[16:17], v[16:17], 0, s[46:47]
	global_load_dword v133, v[16:17], off nt
	v_lshl_add_u64 v[16:17], v[16:17], 0, s[46:47]
	global_load_dword v134, v[16:17], off nt
	v_lshl_add_u64 v[16:17], v[16:17], 0, s[46:47]
	global_load_dword v135, v[16:17], off nt
	v_lshl_add_u64 v[16:17], v[16:17], 0, s[46:47]
	global_load_dword v136, v[16:17], off nt
	v_lshl_add_u64 v[16:17], v[16:17], 0, s[46:47]
	global_load_dword v137, v[16:17], off nt
	v_lshl_add_u64 v[16:17], v[16:17], 0, s[46:47]
	global_load_dword v138, v[16:17], off nt
	v_lshl_add_u64 v[16:17], v[16:17], 0, s[46:47]
	global_load_dword v139, v[16:17], off nt
	v_lshl_add_u64 v[16:17], v[16:17], 0, s[46:47]
	global_load_dword v140, v[16:17], off nt
	v_lshl_add_u64 v[16:17], v[16:17], 0, s[46:47]
	global_load_dword v141, v[16:17], off nt
	v_lshl_add_u64 v[16:17], v[16:17], 0, s[46:47]
	global_load_dword v142, v[16:17], off nt
	v_lshl_add_u64 v[16:17], v[16:17], 0, s[46:47]
	global_load_dword v143, v[16:17], off nt
	v_lshl_add_u64 v[16:17], v[16:17], 0, s[46:47]
	global_load_dword v144, v[16:17], off nt
	v_lshl_add_u64 v[16:17], v[16:17], 0, s[46:47]
	global_load_dword v146, v[16:17], off nt
	v_lshl_add_u64 v[16:17], v[16:17], 0, s[46:47]
	global_load_dword v147, v[16:17], off nt
	v_lshl_add_u64 v[16:17], v[16:17], 0, s[46:47]
	global_load_dword v148, v[16:17], off nt
	v_lshl_add_u64 v[16:17], v[16:17], 0, s[46:47]
	global_load_dword v149, v[16:17], off nt
	v_lshl_add_u64 v[16:17], v[16:17], 0, s[46:47]
	global_load_dword v151, v[16:17], off nt
	v_lshl_add_u64 v[16:17], v[16:17], 0, s[46:47]
	global_load_dword v152, v[16:17], off nt
	v_lshl_add_u64 v[16:17], v[16:17], 0, s[46:47]
	global_load_dword v153, v[16:17], off nt
	v_lshl_add_u64 v[16:17], v[16:17], 0, s[46:47]
	global_load_dword v154, v[16:17], off nt
	v_lshl_add_u64 v[16:17], v[16:17], 0, s[46:47]
	global_load_dword v155, v[16:17], off nt
	v_lshl_add_u64 v[16:17], v[16:17], 0, s[46:47]
	global_load_dword v157, v[16:17], off nt
	v_lshl_add_u64 v[16:17], v[16:17], 0, s[46:47]
	global_load_dword v158, v[16:17], off nt
	v_lshl_add_u64 v[16:17], v[16:17], 0, s[46:47]
	s_mov_b64 exec, s[100:101]
	global_store_dwordx4 v[172:173], v[180:183], off
	global_store_dwordx4 v[174:175], v[184:187], off
	global_store_dwordx4 v[176:177], v[188:191], off
	global_store_dwordx4 v[178:179], v[192:195], off
	s_mov_b64 exec, -1
	s_waitcnt vmcnt(63)
	ds_write2st64_b32 v28, v87, v92 offset1:1
	ds_write2st64_b32 v28, v91, v90 offset0:2 offset1:3
	ds_write2st64_b32 v28, v89, v88 offset0:4 offset1:5
	ds_write2st64_b32 v28, v86, v85 offset0:6 offset1:7
	ds_write2st64_b32 v21, v83, v84 offset0:8 offset1:9
	ds_write2st64_b32 v21, v79, v80 offset0:10 offset1:11
	ds_write2st64_b32 v21, v75, v76 offset0:12 offset1:13
	ds_write2st64_b32 v21, v71, v72 offset0:14 offset1:15
	ds_write2st64_b32 v22, v65, v66 offset0:16 offset1:17
	ds_write2st64_b32 v22, v61, v62 offset0:18 offset1:19
	ds_write2st64_b32 v22, v57, v58 offset0:20 offset1:21
	ds_write2st64_b32 v22, v53, v54 offset0:22 offset1:23
	ds_write2st64_b32 v23, v45, v46 offset0:24 offset1:25
	ds_write2st64_b32 v23, v35, v36 offset0:26 offset1:27
	ds_write2st64_b32 v23, v33, v34 offset0:28 offset1:29
	ds_write2st64_b32 v23, v31, v32 offset0:30 offset1:31
	ds_write2st64_b32 v24, v29, v30 offset0:32 offset1:33
	ds_write2st64_b32 v24, v81, v82 offset0:34 offset1:35
	ds_write2st64_b32 v24, v77, v78 offset0:36 offset1:37
	ds_write2st64_b32 v24, v73, v74 offset0:38 offset1:39
	ds_write2st64_b32 v25, v69, v70 offset0:40 offset1:41
	ds_write2st64_b32 v25, v67, v68 offset0:42 offset1:43
	ds_write2st64_b32 v25, v63, v64 offset0:44 offset1:45
	ds_write2st64_b32 v25, v59, v60 offset0:46 offset1:47
	ds_write2st64_b32 v26, v55, v56 offset0:48 offset1:49
	ds_write2st64_b32 v26, v51, v52 offset0:50 offset1:51
	global_load_dword v159, v[16:17], off nt
	ds_write2st64_b32 v26, v38, v39 offset0:52 offset1:53
	ds_write2st64_b32 v26, v40, v42 offset0:54 offset1:55
	ds_write2st64_b32 v27, v37, v41 offset0:56 offset1:57
	ds_write2st64_b32 v27, v43, v44 offset0:58 offset1:59
	ds_write2st64_b32 v27, v47, v48 offset0:60 offset1:61
	ds_write2st64_b32 v27, v49, v50 offset0:62 offset1:63
	s_waitcnt lgkmcnt(0)
	ds_read2_b32 v[16:17], v1 offset1:32
	v_mov_b32_e32 v30, 0
	ds_read2_b32 v[32:33], v1 offset0:128 offset1:160
	v_mov_b32_e32 v31, 0
	v_add_u32_e32 v145, 0x400, v1
	s_waitcnt lgkmcnt(1)
	v_mul_f32_e32 v4, 0x42800000, v16
	v_mul_f32_e32 v15, 0x42800000, v17
	ds_read2_b32 v[16:17], v1 offset0:64 offset1:96
	v_cvt_pk_fp8_f32 v30, v4, v15
	ds_read2_b32 v[34:35], v145 offset0:128 offset1:160
	v_add_u32_e32 v150, 0x400, v9
	ds_read2_b32 v[38:39], v150 offset0:128 offset1:160
	s_waitcnt lgkmcnt(2)
	v_mul_f32_e32 v4, 0x42800000, v16
	v_mul_f32_e32 v15, 0x42800000, v17
	ds_read2_b32 v[16:17], v1 offset0:192 offset1:224
	v_cvt_pk_fp8_f32 v30, v4, v15 op_sel:[0,0,1]
	v_mul_f32_e32 v4, 0x42800000, v32
	v_mul_f32_e32 v15, 0x42800000, v33
	v_cvt_pk_fp8_f32 v31, v4, v15
	s_waitcnt lgkmcnt(0)
	v_mul_f32_e32 v4, 0x42800000, v16
	v_mul_f32_e32 v15, 0x42800000, v17
	ds_read2_b32 v[16:17], v145 offset0:64 offset1:96
	ds_read2_b32 v[32:33], v145 offset1:32
	v_cvt_pk_fp8_f32 v31, v4, v15 op_sel:[0,0,1]
	v_lshl_add_u64 v[10:11], v[10:11], 0, v[6:7]
	v_add_u32_e32 v156, 0x400, v18
	s_waitcnt lgkmcnt(1)
	v_mul_f32_e32 v29, 0x42800000, v16
	v_mul_f32_e32 v36, 0x42800000, v17
	ds_read2_b32 v[16:17], v145 offset0:192 offset1:224
	s_waitcnt lgkmcnt(1)
	v_mul_f32_e32 v4, 0x42800000, v32
	v_mul_f32_e32 v15, 0x42800000, v33
	v_mov_b32_e32 v32, 0
	v_cvt_pk_fp8_f32 v32, v4, v15
	v_mul_f32_e32 v4, 0x42800000, v34
	v_mul_f32_e32 v15, 0x42800000, v35
	v_mov_b32_e32 v33, 0
	ds_read2_b32 v[34:35], v9 offset1:32
	v_cvt_pk_fp8_f32 v33, v4, v15
	s_waitcnt lgkmcnt(1)
	v_mul_f32_e32 v4, 0x42800000, v16
	v_mul_f32_e32 v15, 0x42800000, v17
	ds_read2_b32 v[16:17], v9 offset0:64 offset1:96
	v_cvt_pk_fp8_f32 v32, v29, v36 op_sel:[0,0,1]
	ds_read2_b32 v[36:37], v9 offset0:128 offset1:160
	v_cvt_pk_fp8_f32 v33, v4, v15 op_sel:[0,0,1]
	s_waitcnt lgkmcnt(2)
	v_mul_f32_e32 v4, 0x42800000, v34
	v_mul_f32_e32 v15, 0x42800000, v35
	v_mov_b32_e32 v34, 0
	v_cvt_pk_fp8_f32 v34, v4, v15
	s_waitcnt lgkmcnt(1)
	v_mul_f32_e32 v4, 0x42800000, v16
	v_mul_f32_e32 v15, 0x42800000, v17
	ds_read2_b32 v[16:17], v9 offset0:192 offset1:224
	s_waitcnt lgkmcnt(1)
	v_mul_f32_e32 v29, 0x42800000, v36
	v_mul_f32_e32 v36, 0x42800000, v37
	v_mov_b32_e32 v35, 0
	v_cvt_pk_fp8_f32 v35, v29, v36
	ds_read2_b32 v[36:37], v150 offset1:32
	v_cvt_pk_fp8_f32 v34, v4, v15 op_sel:[0,0,1]
	s_waitcnt lgkmcnt(1)
	v_mul_f32_e32 v4, 0x42800000, v16
	v_mul_f32_e32 v15, 0x42800000, v17
	ds_read2_b32 v[16:17], v150 offset0:64 offset1:96
	v_cvt_pk_fp8_f32 v35, v4, v15 op_sel:[0,0,1]
	s_waitcnt lgkmcnt(1)
	v_mul_f32_e32 v4, 0x42800000, v36
	v_mul_f32_e32 v15, 0x42800000, v37
	v_mov_b32_e32 v36, 0
	v_cvt_pk_fp8_f32 v36, v4, v15
	s_waitcnt lgkmcnt(0)
	v_mul_f32_e32 v4, 0x42800000, v16
	v_mul_f32_e32 v15, 0x42800000, v17
	ds_read2_b32 v[16:17], v150 offset0:192 offset1:224
	v_cvt_pk_fp8_f32 v36, v4, v15 op_sel:[0,0,1]
	v_mul_f32_e32 v4, 0x42800000, v38
	v_mul_f32_e32 v15, 0x42800000, v39
	v_mov_b32_e32 v37, 0
	v_cvt_pk_fp8_f32 v37, v4, v15
	s_waitcnt lgkmcnt(0)
; __device__ __forceinline__ MoeItem moe_item(const float* wg, const float* wu, const float* wd, const float* win, const float* wout, const float* wpn, const float* wpd, unsigned char* ws, int r, int lane) {
;     ...
;     const int mat = r / MOE_IE, q = r % MOE_IE, e = mat / 3, which = mat % 3, kb = q / 64, nb = q % 64, n0 = nb * 32;
;     const float* src = (which == 0 ? wg : (which == 1 ? wu : wd)) + (size_t)e * DM * DFF + (size_t)(kb * 128 + (lane >> 5)) * DFF + n0 + (lane & 31);
;     unsigned char* dst;
;     if (which < 2) dst = ws + WS_WGUT + ((size_t)(e * 16 + (n0 >> 7)) * 256 + which * 128 + (n0 & 127)) * DM;
;     else dst = ws + WS_WDT + ((size_t)e * DM + n0) * DFF;
;     MoeItem it; it.stride = DFF; it.dpitch = DM; it.src = src; it.dst = dst + kb * 128 + (size_t)(lane >> 3) * DM + 16 * (lane & 7); return it;
	v_mul_f32_e32 v4, 0x42800000, v16
	v_mul_f32_e32 v15, 0x42800000, v17
	ds_read2_b32 v[16:17], v18 offset1:32
	v_cvt_pk_fp8_f32 v37, v4, v15 op_sel:[0,0,1]
	s_nop 0
	v_mov_b64_e32 v[196:197], v[10:11]
	v_mov_b64_e32 v[204:205], v[30:31]
	v_mov_b64_e32 v[206:207], v[32:33]
	ds_read2_b32 v[32:33], v18 offset0:64 offset1:96
	s_lshl_b64 s[38:39], s[38:39], 3
	s_waitcnt lgkmcnt(1)
	v_mul_f32_e32 v4, 0x42800000, v16
	v_mul_f32_e32 v15, 0x42800000, v17
	ds_read2_b32 v[16:17], v18 offset0:128 offset1:160
	v_mov_b32_e32 v30, 0
	v_cvt_pk_fp8_f32 v30, v4, v15
	s_waitcnt lgkmcnt(1)
	v_mul_f32_e32 v4, 0x42800000, v32
	v_mov_b32_e32 v31, 0
	s_waitcnt lgkmcnt(0)
	v_mul_f32_e32 v29, 0x42800000, v16
	v_mul_f32_e32 v32, 0x42800000, v17
	ds_read2_b32 v[16:17], v18 offset0:192 offset1:224
	v_mul_f32_e32 v15, 0x42800000, v33
	v_cvt_pk_fp8_f32 v31, v29, v32
	ds_read2_b32 v[32:33], v156 offset1:32
	v_cvt_pk_fp8_f32 v30, v4, v15 op_sel:[0,0,1]
	s_waitcnt lgkmcnt(1)
	v_mul_f32_e32 v4, 0x42800000, v16
	v_mul_f32_e32 v15, 0x42800000, v17
	ds_read2_b32 v[16:17], v156 offset0:64 offset1:96
	v_lshl_add_u64 v[10:11], v[10:11], 0, s[38:39]
	s_nop 0
	v_mov_b64_e32 v[198:199], v[10:11]
	v_mov_b64_e32 v[208:209], v[34:35]
	v_mov_b64_e32 v[210:211], v[36:37]
	ds_read2_b32 v[34:35], v156 offset0:128 offset1:160
	v_cvt_pk_fp8_f32 v31, v4, v15 op_sel:[0,0,1]
	s_waitcnt lgkmcnt(2)
	v_mul_f32_e32 v4, 0x42800000, v32
	v_mul_f32_e32 v15, 0x42800000, v33
	v_mov_b32_e32 v32, 0
	v_cvt_pk_fp8_f32 v32, v4, v15
	s_waitcnt lgkmcnt(1)
	v_mul_f32_e32 v4, 0x42800000, v16
	v_mul_f32_e32 v15, 0x42800000, v17
	ds_read2_b32 v[16:17], v156 offset0:192 offset1:224
	s_waitcnt lgkmcnt(1)
	v_mul_f32_e32 v29, 0x42800000, v34
	v_mul_f32_e32 v34, 0x42800000, v35
	v_mov_b32_e32 v33, 0
	v_cvt_pk_fp8_f32 v33, v29, v34
	ds_read2_b32 v[34:35], v19 offset1:32
	v_cvt_pk_fp8_f32 v32, v4, v15 op_sel:[0,0,1]
	s_waitcnt lgkmcnt(1)
	v_mul_f32_e32 v4, 0x42800000, v16
	v_mul_f32_e32 v15, 0x42800000, v17
	ds_read2_b32 v[16:17], v19 offset0:64 offset1:96
	ds_read2_b32 v[36:37], v19 offset0:128 offset1:160
	v_cvt_pk_fp8_f32 v33, v4, v15 op_sel:[0,0,1]
	s_waitcnt lgkmcnt(2)
	v_mul_f32_e32 v4, 0x42800000, v34
	v_mul_f32_e32 v15, 0x42800000, v35
	v_mov_b32_e32 v34, 0
	v_cvt_pk_fp8_f32 v34, v4, v15
	s_waitcnt lgkmcnt(1)
	v_mul_f32_e32 v4, 0x42800000, v16
	v_mul_f32_e32 v15, 0x42800000, v17
	ds_read2_b32 v[16:17], v19 offset0:192 offset1:224
	s_waitcnt lgkmcnt(1)
	v_mul_f32_e32 v29, 0x42800000, v36
	v_mul_f32_e32 v36, 0x42800000, v37
	v_mov_b32_e32 v35, 0
	v_add_u32_e32 v160, 0x400, v19
	v_cvt_pk_fp8_f32 v35, v29, v36
	ds_read2_b32 v[36:37], v160 offset1:32
	v_cvt_pk_fp8_f32 v34, v4, v15 op_sel:[0,0,1]
	s_waitcnt lgkmcnt(1)
	v_mul_f32_e32 v4, 0x42800000, v16
	v_mul_f32_e32 v15, 0x42800000, v17
	ds_read2_b32 v[16:17], v160 offset0:64 offset1:96
	ds_read2_b32 v[38:39], v160 offset0:128 offset1:160
	v_cvt_pk_fp8_f32 v35, v4, v15 op_sel:[0,0,1]
	s_waitcnt lgkmcnt(2)
	v_mul_f32_e32 v4, 0x42800000, v36
	v_mul_f32_e32 v15, 0x42800000, v37
	v_mov_b32_e32 v36, 0
	v_cvt_pk_fp8_f32 v36, v4, v15
	s_waitcnt lgkmcnt(1)
	v_mul_f32_e32 v4, 0x42800000, v16
	v_mul_f32_e32 v15, 0x42800000, v17
	ds_read2_b32 v[16:17], v160 offset0:192 offset1:224
	s_waitcnt lgkmcnt(1)
	v_mul_f32_e32 v29, 0x42800000, v38
	v_mul_f32_e32 v38, 0x42800000, v39
	v_mov_b32_e32 v37, 0
	v_cvt_pk_fp8_f32 v37, v29, v38
	v_cvt_pk_fp8_f32 v36, v4, v15 op_sel:[0,0,1]
	s_waitcnt lgkmcnt(0)
	v_mul_f32_e32 v4, 0x42800000, v16
	v_mul_f32_e32 v15, 0x42800000, v17
	v_cvt_pk_fp8_f32 v37, v4, v15 op_sel:[0,0,1]
	v_lshl_add_u64 v[10:11], v[10:11], 0, s[38:39]
	s_nop 0
	v_mov_b64_e32 v[200:201], v[10:11]
	v_mov_b64_e32 v[212:213], v[30:31]
	v_mov_b64_e32 v[214:215], v[32:33]
	v_lshl_add_u64 v[10:11], v[10:11], 0, s[38:39]
	s_nop 0
	v_mov_b64_e32 v[202:203], v[10:11]
	v_mov_b64_e32 v[216:217], v[34:35]
	v_mov_b64_e32 v[218:219], v[36:37]
	s_waitcnt lgkmcnt(0)
	s_add_i32 s3, s89, s3
	s_min_i32 s43, s3, s7
	s_cmp_lt_i32 s43, 0x19000
	s_mov_b64 s[38:39], -1
	s_cbranch_scc0 .LBB0_126
	s_cmp_lt_i32 s43, 0x18c00
	s_cbranch_scc0 .LBB0_123
	s_cmp_lt_i32 s43, 0x18000
	s_cbranch_scc0 .LBB0_113
	s_ashr_i32 s4, s43, 31
	s_lshr_b32 s4, s4, 22
	s_add_i32 s4, s43, s4
	s_ashr_i32 s39, s4, 10
	s_and_b32 s4, s4, 0xfc00
	s_sub_i32 s46, s43, s4
	s_mul_hi_i32 s4, s43, 0x2aaaaaab
	s_lshr_b32 s38, s4, 31
	s_ashr_i32 s4, s4, 9
	s_add_i32 s38, s4, s38
	s_mul_hi_i32 s4, s39, 0x55555556
	s_lshr_b32 s45, s4, 31
	s_add_i32 s4, s4, s45
	s_mul_i32 s4, s4, 3
	s_sub_i32 s4, s39, s4
	s_sext_i32_i16 s39, s46
	s_bfe_u32 s39, s39, 0x60019
	s_add_i32 s45, s46, s39
	s_and_b32 s39, s45, 0xffc0
	s_sub_i32 s39, s46, s39
	s_sext_i32_i16 s84, s39
	s_lshl_b32 s46, s84, 5
	s_ashr_i32 s39, s38, 31
	s_ashr_i32 s47, s46, 31
	s_cmp_gt_i32 s4, 1
	s_mov_b64 s[70:71], -1
	s_cbranch_scc0 .LBB0_110
	s_lshl_b64 s[68:69], s[38:39], 22
	s_lshl_b64 s[70:71], s[46:47], 11
	s_add_u32 s68, s73, s68
	s_addc_u32 s69, s74, s69
	s_add_u32 s68, s68, s70
	s_addc_u32 s69, s69, s71
	s_mov_b64 s[70:71], 0

; __device__ __forceinline__ unsigned f2bf(float f) { unsigned u = __float_as_uint(f); return (u + 0x7fffu + ((u >> 16) & 1u)) >> 16; }
;     ...
;     }
;     const int gt = F.vcu * 512 + F.tid, NGT = F.G * 512;
;     if (parts & 4) for (int i = gt; i < 32 * 2048; i += NGT) { const int e = i >> 11, k = i & 2047; const float w = F.in[I_WR][k * 32 + e]; const unsigned hb = f2bf(w); const float lo = w - __uint_as_float(hb << 16);
;         ((bf16_t*)(F.ws + WS_WRT))[i] = (bf16_t)hb; ((bf16_t*)(F.ws + WS_WRT))[65536 + i] = (bf16_t)f2bf(lo); }
.LBB0_130:
	s_mov_b64 exec, s[100:101]
	global_store_dwordx4 v[172:173], v[180:183], off
	global_store_dwordx4 v[174:175], v[184:187], off
	global_store_dwordx4 v[176:177], v[188:191], off
	global_store_dwordx4 v[178:179], v[192:195], off
	s_mov_b64 exec, -1
	v_readlane_b32 s3, v255, 2
	s_nop 1
	v_lshl_or_b32 v2, s3, 9, v0
	s_mov_b32 s3, 0x10000
	v_cmp_gt_i32_e32 vcc, s3, v2
	v_ashrrev_i32_e32 v3, 31, v2
	s_and_saveexec_b64 s[4:5], vcc
	s_cbranch_execz .LBB0_133
	s_lshl_b32 s16, s33, 9
	v_lshl_add_u64 v[4:5], v[2:3], 1, s[82:83]
	s_mov_b64 s[6:7], 0x3c00000
	s_ashr_i32 s17, s16, 31
	v_lshlrev_b32_e32 v1, 5, v0
	v_readlane_b32 s3, v255, 2
	v_lshl_add_u64 v[4:5], v[4:5], 0, s[6:7]
	s_lshl_b64 s[20:21], s[16:17], 1
	v_lshl_or_b32 v1, s3, 14, v1
	s_lshl_b32 s3, s33, 14
	s_mov_b64 s[24:25], 0
	s_movk_i32 s6, 0x7fff
	s_mov_b32 s7, 0xffff
	v_mov_b32_e32 v6, v2

; __global__ void __launch_bounds__(512, 2) fwd(Args args) {
	.amdhsa_kernel _Z3fwd4Args
		.amdhsa_group_segment_fixed_size 0
		.amdhsa_private_segment_fixed_size 0
		.amdhsa_kernarg_size 504
		.amdhsa_user_sgpr_count 2
		.amdhsa_user_sgpr_dispatch_ptr 0
		.amdhsa_user_sgpr_queue_ptr 0
		.amdhsa_user_sgpr_kernarg_segment_ptr 1
		.amdhsa_user_sgpr_dispatch_id 0
		.amdhsa_user_sgpr_kernarg_preload_length 0
		.amdhsa_user_sgpr_kernarg_preload_offset 0
		.amdhsa_user_sgpr_private_segment_size 0
		.amdhsa_uses_dynamic_stack 0
		.amdhsa_enable_private_segment 0
		.amdhsa_system_sgpr_workgroup_id_x 1
		.amdhsa_system_sgpr_workgroup_id_y 0
		.amdhsa_system_sgpr_workgroup_id_z 0
		.amdhsa_system_sgpr_workgroup_info 0
		.amdhsa_system_vgpr_workitem_id 0
		.amdhsa_next_free_vgpr 256
		.amdhsa_next_free_sgpr 102
		.amdhsa_accum_offset 256
		.amdhsa_reserve_vcc 1
		.amdhsa_float_round_mode_32 0
		.amdhsa_float_round_mode_16_64 0
		.amdhsa_float_denorm_mode_32 3
		.amdhsa_float_denorm_mode_16_64 3
		.amdhsa_dx10_clamp 1
		.amdhsa_ieee_mode 1
		.amdhsa_fp16_overflow 0
		.amdhsa_tg_split 0
		.amdhsa_exception_fp_ieee_invalid_op 0
		.amdhsa_exception_fp_denorm_src 0
		.amdhsa_exception_fp_ieee_div_zero 0
		.amdhsa_exception_fp_ieee_overflow 0
		.amdhsa_exception_fp_ieee_underflow 0
		.amdhsa_exception_fp_ieee_inexact 0
		.amdhsa_exception_int_div_zero 0
	.end_amdhsa_kernel

; __global__ void __launch_bounds__(512, 2) fwd(Args args) {
amdhsa.kernels:
  - .agpr_count:     0
    .args:
      - .offset:         0
        .size:           248
        .value_kind:     by_value
      - .offset:         248
        .size:           4
        .value_kind:     hidden_block_count_x
      - .offset:         252
        .size:           4
        .value_kind:     hidden_block_count_y
      - .offset:         256
        .size:           4
        .value_kind:     hidden_block_count_z
      - .offset:         260
        .size:           2
        .value_kind:     hidden_group_size_x
      - .offset:         262
        .size:           2
        .value_kind:     hidden_group_size_y
      - .offset:         264
        .size:           2
        .value_kind:     hidden_group_size_z
      - .offset:         266
        .size:           2
        .value_kind:     hidden_remainder_x
      - .offset:         268
        .size:           2
        .value_kind:     hidden_remainder_y
      - .offset:         270
        .size:           2
        .value_kind:     hidden_remainder_z
      - .offset:         288
        .size:           8
        .value_kind:     hidden_global_offset_x
      - .offset:         296
        .size:           8
        .value_kind:     hidden_global_offset_y
      - .offset:         304
        .size:           8
        .value_kind:     hidden_global_offset_z
      - .offset:         312
        .size:           2
        .value_kind:     hidden_grid_dims
      - .offset:         368
        .size:           4
        .value_kind:     hidden_dynamic_lds_size
    .group_segment_fixed_size: 0
    .kernarg_segment_align: 8
    .kernarg_segment_size: 504
    .language:       OpenCL C
    .language_version:
      - 2
      - 0
    .max_flat_workgroup_size: 512
    .name:           _Z3fwd4Args
    .private_segment_fixed_size: 0
    .sgpr_count:     108
    .sgpr_spill_count: 12
    .symbol:         _Z3fwd4Args.kd
    .uniform_work_group_size: 1
    .uses_dynamic_stack: false
    .vgpr_count:     256
    .vgpr_spill_count: 0
    .wavefront_size: 64
